# v12 + P9 stage C: the residual x1 dword of each visit is requested at the start of the visit (fresh registers) instead of mid-reduction
# speedup vs baseline: 1.0054x; 1.0042x over previous
.LBB0_1314:
	v_perm_b32 v202, v54, v50, s75
	v_perm_b32 v50, v54, v50, s76
	v_perm_b32 v54, v62, v58, s75
	v_perm_b32 v58, v62, v58, s76
	v_perm_b32 v62, v54, v202, s77
	v_mov_b32_e32 v203, 0
	s_waitcnt lgkmcnt(0)
	v_dot4c_i32_i8_e32 v203, v62, v156
	v_perm_b32 v54, v54, v202, s78
	v_mov_b32_e32 v62, 0
	v_dot4c_i32_i8_e32 v62, v54, v156
	v_perm_b32 v54, v58, v50, s77
	v_mov_b32_e32 v202, 0
	v_dot4c_i32_i8_e32 v202, v54, v156
	v_perm_b32 v50, v58, v50, s78
	v_mov_b32_e32 v54, 0
	v_dot4c_i32_i8_e32 v54, v50, v156
	v_perm_b32 v50, v55, v51, s75
	v_perm_b32 v51, v55, v51, s76
	v_perm_b32 v55, v63, v59, s75
	v_perm_b32 v58, v63, v59, s76
	v_perm_b32 v59, v55, v50, s77
	v_mov_b32_e32 v63, 0
	v_perm_b32 v50, v55, v50, s78
	v_mov_b32_e32 v55, 0
	v_dot4c_i32_i8_e32 v63, v59, v156
	v_dot4c_i32_i8_e32 v55, v50, v156
	v_perm_b32 v50, v58, v51, s77
	v_mov_b32_e32 v59, 0
	v_dot4c_i32_i8_e32 v59, v50, v156
	v_perm_b32 v50, v58, v51, s78
	v_mov_b32_e32 v51, 0
	v_dot4c_i32_i8_e32 v51, v50, v156
	v_perm_b32 v50, v56, v52, s75
	v_perm_b32 v52, v56, v52, s76
	v_perm_b32 v56, v64, v60, s75
	v_perm_b32 v58, v64, v60, s76
	v_perm_b32 v60, v56, v50, s77
	v_mov_b32_e32 v64, 0
	v_perm_b32 v50, v56, v50, s78
	v_mov_b32_e32 v56, 0
	v_dot4c_i32_i8_e32 v64, v60, v156
	v_dot4c_i32_i8_e32 v56, v50, v156
	v_perm_b32 v50, v58, v52, s77
	v_mov_b32_e32 v60, 0
	v_dot4c_i32_i8_e32 v60, v50, v156
	v_perm_b32 v50, v58, v52, s78
	v_mov_b32_e32 v52, 0
	v_dot4c_i32_i8_e32 v52, v50, v156
	v_perm_b32 v50, v57, v53, s75
	v_perm_b32 v53, v57, v53, s76
	v_perm_b32 v57, v65, v61, s75
	v_perm_b32 v58, v65, v61, s76
	v_perm_b32 v61, v57, v50, s77
	v_mov_b32_e32 v65, 0
	v_perm_b32 v50, v57, v50, s78
	v_mov_b32_e32 v57, 0
	v_dot4c_i32_i8_e32 v65, v61, v156
	v_dot4c_i32_i8_e32 v57, v50, v156
	v_perm_b32 v50, v58, v53, s77
	v_mov_b32_e32 v61, 0
	v_dot4c_i32_i8_e32 v61, v50, v156
	v_perm_b32 v50, v58, v53, s78
	v_mov_b32_e32 v53, 0
	v_dot4c_i32_i8_e32 v53, v50, v156
	v_perm_b32 v50, v38, v34, s75
	v_perm_b32 v34, v38, v34, s76
	v_perm_b32 v38, v46, v42, s75
	v_perm_b32 v42, v46, v42, s76
	v_perm_b32 v46, v38, v50, s77
	v_perm_b32 v38, v38, v50, s78
	v_dot4c_i32_i8_e32 v62, v38, v157
	v_perm_b32 v38, v42, v34, s77
	v_perm_b32 v34, v42, v34, s78
	v_dot4c_i32_i8_e32 v202, v38, v157
	v_dot4c_i32_i8_e32 v54, v34, v157
	v_perm_b32 v34, v39, v35, s75
	v_perm_b32 v38, v47, v43, s75
	v_perm_b32 v35, v39, v35, s76
	v_perm_b32 v39, v47, v43, s76
	v_perm_b32 v42, v38, v34, s77
	v_perm_b32 v34, v38, v34, s78
	v_dot4c_i32_i8_e32 v55, v34, v157
	v_perm_b32 v34, v39, v35, s77
	v_dot4c_i32_i8_e32 v59, v34, v157
	v_perm_b32 v34, v39, v35, s78
	v_dot4c_i32_i8_e32 v51, v34, v157
	v_perm_b32 v34, v40, v36, s75
	v_perm_b32 v35, v40, v36, s76
	v_perm_b32 v36, v48, v44, s75
	v_perm_b32 v38, v48, v44, s76
	v_perm_b32 v39, v36, v34, s77
	v_perm_b32 v34, v36, v34, s78
	v_dot4c_i32_i8_e32 v56, v34, v157
	v_perm_b32 v34, v38, v35, s77
	v_dot4c_i32_i8_e32 v60, v34, v157
	v_perm_b32 v34, v38, v35, s78
	v_dot4c_i32_i8_e32 v52, v34, v157
	v_perm_b32 v34, v41, v37, s75
	v_perm_b32 v36, v49, v45, s75
	v_perm_b32 v35, v41, v37, s76
	v_perm_b32 v37, v49, v45, s76
	v_perm_b32 v38, v36, v34, s77
	v_perm_b32 v34, v36, v34, s78
	v_dot4c_i32_i8_e32 v57, v34, v157
	v_perm_b32 v34, v37, v35, s77
	v_dot4c_i32_i8_e32 v61, v34, v157
	v_perm_b32 v34, v37, v35, s78
	v_dot4c_i32_i8_e32 v53, v34, v157
	ds_read_b64 v[34:35], v201 offset:64
	v_dot4c_i32_i8_e32 v65, v38, v157
	v_perm_b32 v36, v82, v86, s75
	v_perm_b32 v38, v90, v94, s75
	v_dot4c_i32_i8_e32 v64, v39, v157
	v_perm_b32 v37, v82, v86, s76
	v_perm_b32 v39, v90, v94, s76
	v_perm_b32 v40, v38, v36, s77
	v_perm_b32 v36, v38, v36, s78
	s_waitcnt lgkmcnt(0)
	v_dot4c_i32_i8_e32 v62, v36, v34
	v_perm_b32 v36, v39, v37, s77
	v_dot4c_i32_i8_e32 v202, v36, v34
	v_perm_b32 v36, v39, v37, s78
	v_dot4c_i32_i8_e32 v203, v46, v157
	v_dot4c_i32_i8_e32 v54, v36, v34
	v_perm_b32 v36, v83, v87, s75
	v_perm_b32 v38, v91, v95, s75
	v_dot4c_i32_i8_e32 v203, v40, v34
	v_perm_b32 v37, v83, v87, s76
	v_perm_b32 v39, v91, v95, s76
	v_perm_b32 v40, v38, v36, s77
	v_perm_b32 v36, v38, v36, s78
	v_dot4c_i32_i8_e32 v55, v36, v34
	v_perm_b32 v36, v39, v37, s77
	v_dot4c_i32_i8_e32 v59, v36, v34
	v_perm_b32 v36, v39, v37, s78
	v_dot4c_i32_i8_e32 v63, v42, v157
	v_dot4c_i32_i8_e32 v51, v36, v34
	v_perm_b32 v36, v84, v88, s75
	v_perm_b32 v38, v92, v96, s75
	v_dot4c_i32_i8_e32 v63, v40, v34
	v_perm_b32 v37, v84, v88, s76
	v_perm_b32 v39, v92, v96, s76
	v_perm_b32 v40, v38, v36, s77
	v_perm_b32 v36, v38, v36, s78
	v_dot4c_i32_i8_e32 v56, v36, v34
	v_perm_b32 v36, v39, v37, s77
	v_dot4c_i32_i8_e32 v60, v36, v34
	v_perm_b32 v36, v39, v37, s78
	v_dot4c_i32_i8_e32 v52, v36, v34
	v_perm_b32 v36, v85, v89, s75
	v_perm_b32 v38, v93, v97, s75
	v_dot4c_i32_i8_e32 v64, v40, v34
	v_perm_b32 v37, v85, v89, s76
	v_perm_b32 v39, v93, v97, s76
	v_perm_b32 v40, v38, v36, s77
	v_perm_b32 v36, v38, v36, s78
	v_dot4c_i32_i8_e32 v57, v36, v34
	v_perm_b32 v36, v39, v37, s77
	v_dot4c_i32_i8_e32 v61, v36, v34
	v_perm_b32 v36, v39, v37, s78
	v_dot4c_i32_i8_e32 v65, v40, v34
	v_dot4c_i32_i8_e32 v53, v36, v34
	v_perm_b32 v34, v66, v70, s75
	v_perm_b32 v37, v74, v78, s75
	v_perm_b32 v36, v66, v70, s76
	v_perm_b32 v38, v74, v78, s76
	v_perm_b32 v39, v37, v34, s77
	v_perm_b32 v34, v37, v34, s78
	v_dot4c_i32_i8_e32 v62, v34, v35
	v_perm_b32 v34, v38, v36, s77
	v_dot4c_i32_i8_e32 v202, v34, v35
	v_perm_b32 v34, v38, v36, s78
	s_or_b32 s15, s44, s29
	v_dot4c_i32_i8_e32 v54, v34, v35
	v_perm_b32 v34, v67, v71, s75
	v_perm_b32 v37, v75, v79, s75
	s_add_i32 s14, s15, s22
	s_add_i32 s44, s23, 32
	s_lshl_b32 s15, s15, 2
	v_dot4c_i32_i8_e32 v203, v39, v35
	v_perm_b32 v39, v37, v34, s77
	s_and_b32 s44, s44, 0xf80
	s_add_i32 s15, s15, 0
	v_dot4c_i32_i8_e32 v63, v39, v35
	v_or_b32_e32 v39, s44, v163
	s_add_i32 s44, s15, 0x14000
	s_ashr_i32 s15, s14, 31
	s_lshl_b64 s[14:15], s[14:15], 12
	s_add_u32 s14, s60, s14
	s_addc_u32 s15, s61, s15
	v_lshlrev_b32_e32 v42, 1, v39
	v_perm_b32 v36, v67, v71, s76
	v_perm_b32 v38, v75, v79, s76
	v_perm_b32 v34, v37, v34, s78
	v_dot4c_i32_i8_e32 v55, v34, v35
	v_perm_b32 v34, v38, v36, s77
	v_dot4c_i32_i8_e32 v59, v34, v35
	v_perm_b32 v34, v38, v36, s78
	v_dot4c_i32_i8_e32 v51, v34, v35
	v_perm_b32 v34, v68, v72, s75
	v_perm_b32 v37, v76, v80, s75
	v_perm_b32 v36, v68, v72, s76
	v_perm_b32 v38, v76, v80, s76
	v_perm_b32 v40, v37, v34, s77
	v_perm_b32 v34, v37, v34, s78
	v_dot4c_i32_i8_e32 v56, v34, v35
	v_perm_b32 v34, v38, v36, s77
	v_dot4c_i32_i8_e32 v60, v34, v35
	v_perm_b32 v34, v38, v36, s78
	v_dot4c_i32_i8_e32 v52, v34, v35
	v_perm_b32 v34, v69, v73, s75
	v_perm_b32 v37, v77, v81, s75
	v_dot4c_i32_i8_e32 v64, v40, v35
	v_perm_b32 v36, v69, v73, s76
	v_perm_b32 v38, v77, v81, s76
	v_perm_b32 v40, v37, v34, s77
	v_perm_b32 v34, v37, v34, s78
	v_dot4c_i32_i8_e32 v57, v34, v35
	v_perm_b32 v34, v38, v36, s77
	v_dot4c_i32_i8_e32 v61, v34, v35
	v_perm_b32 v34, v38, v36, s78
	v_dot4c_i32_i8_e32 v65, v40, v35
	v_dot4c_i32_i8_e32 v53, v34, v35
	v_permlane32_swap_b32_e32 v203, v64
	v_permlane32_swap_b32_e32 v62, v56
	v_permlane32_swap_b32_e32 v202, v60
	v_permlane32_swap_b32_e32 v54, v52
	v_permlane32_swap_b32_e32 v63, v65
	v_permlane32_swap_b32_e32 v55, v57
	v_permlane32_swap_b32_e32 v59, v61
	v_permlane32_swap_b32_e32 v51, v53
	v_add_u32_e32 v35, v203, v64
	v_add_u32_e32 v36, v62, v56
	v_add_u32_e32 v37, v202, v60
	v_add_u32_e32 v38, v54, v52
	v_add_u32_e32 v40, v63, v65
	v_add_u32_e32 v43, v55, v57
	v_add_u32_e32 v44, v59, v61
	v_add_u32_e32 v45, v51, v53
	v_permlane16_swap_b32_e32 v35, v40
	v_permlane16_swap_b32_e32 v36, v43
	v_permlane16_swap_b32_e32 v37, v44
	v_permlane16_swap_b32_e32 v38, v45
	v_add_u32_e32 v36, v36, v43
	v_add_u32_e32 v35, v35, v40
	v_add_u32_e32 v38, v38, v45
	v_add_u32_e32 v37, v37, v44
	v_mov_b32_e32 v34, s44
	v_cndmask_b32_e64 v40, v35, v37, s[12:13]
	v_cndmask_b32_e64 v43, v38, v36, s[12:13]
	v_cndmask_b32_e64 v35, v37, v35, s[12:13]
	v_cndmask_b32_e64 v36, v36, v38, s[12:13]
	ds_read_b32 v34, v34
	v_lshl_add_u32 v39, v39, 2, 0
	v_add_u32_dpp v35, v40, v35 row_ror:8 row_mask:0xf bank_mask:0xf bound_ctrl:1
	v_add_u32_dpp v38, v36, v43 row_ror:8 row_mask:0xf bank_mask:0xf bound_ctrl:1
	ds_read_b64 v[36:37], v39 offset:32768
	v_cvt_f32_i32_e32 v39, v38
	v_cvt_f32_i32_e32 v38, v35
	s_waitcnt vmcnt(0)
	v_lshlrev_b32_e32 v40, 16, v213
	v_and_b32_e32 v41, 0xffff0000, v213
	v_mov_b64_e32 v[50:51], v[102:103]
	s_waitcnt lgkmcnt(1)
	v_pk_mul_f32 v[34:35], v[34:35], v[38:39] op_sel_hi:[0,1]
	s_waitcnt lgkmcnt(0)
	v_pk_fma_f32 v[34:35], v[34:35], v[36:37], v[40:41]
	v_mov_b64_e32 v[54:55], v[98:99]
	v_and_b32_sdwa v37, v34, v199 dst_sel:DWORD dst_unused:UNUSED_PAD src0_sel:WORD_1 src1_sel:DWORD
	v_and_b32_sdwa v36, v35, v199 dst_sel:DWORD dst_unused:UNUSED_PAD src0_sel:WORD_1 src1_sel:DWORD
	v_add3_u32 v34, v34, v37, s80
	v_add3_u32 v35, v35, v36, s80
	v_lshrrev_b32_e32 v34, 16, v34
	v_and_or_b32 v34, v35, s79, v34
	global_store_dword v42, v34, s[14:15]
	v_mov_b64_e32 v[58:59], v[110:111]
	v_mov_b64_e32 v[62:63], v[106:107]
	v_mov_b64_e32 v[34:35], v[118:119]
	v_mov_b64_e32 v[38:39], v[114:115]
	v_mov_b64_e32 v[42:43], v[126:127]
	v_mov_b64_e32 v[46:47], v[122:123]
	v_mov_b64_e32 v[52:53], v[104:105]
	v_mov_b64_e32 v[56:57], v[100:101]
	v_mov_b64_e32 v[60:61], v[112:113]
	v_mov_b64_e32 v[64:65], v[108:109]
	v_mov_b64_e32 v[36:37], v[120:121]
	v_mov_b64_e32 v[40:41], v[116:117]
	v_mov_b64_e32 v[44:45], v[128:129]
	v_mov_b64_e32 v[48:49], v[124:125]

.LBB0_1321:
	s_or_b32 s84, s44, s29
	s_add_i32 s84, s84, s22
	s_ashr_i32 s85, s84, 31
	s_lshl_b64 s[84:85], s[84:85], 12
	s_add_u32 s84, s60, s84
	s_addc_u32 s85, s61, s85
	s_and_b32 s86, s23, 0x780
	v_or_b32_e32 v208, s86, v163
	v_lshlrev_b32_e32 v208, 1, v208
	global_load_dword v209, v208, s[84:85]
	s_add_i32 s14, s23, 16
	s_and_b32 s81, s14, 0xf80
	s_add_u32 s14, s18, s81
	s_addc_u32 s15, s19, 0
	s_add_i32 s45, s46, 0xfffffec0
	s_and_b32 s45, s45, 0x380
	v_lshl_add_u32 v66, s45, 1, v181
	ds_read_b128 v[66:69], v66
	v_lshl_add_u32 v72, s44, 7, v186
	ds_read_b64 v[70:71], v72
	v_mov_b32_e32 v74, 0
	v_mov_b32_e32 v76, 0
	s_waitcnt lgkmcnt(1)
	v_lshlrev_b32_e32 v73, 11, v66
	v_bfe_u32 v66, v66, 16, 16
	v_and_or_b32 v73, v73, s74, v130
	v_lshl_or_b32 v66, v66, 11, v130
	global_load_dwordx4 v[114:117], v73, s[14:15]
	global_load_dwordx4 v[118:121], v66, s[14:15]
	v_lshlrev_b32_e32 v66, 11, v67
	v_and_or_b32 v66, v66, s74, v130
	v_bfe_u32 v67, v67, 16, 16
	v_lshl_or_b32 v67, v67, 11, v130
	global_load_dwordx4 v[122:125], v66, s[14:15]
	global_load_dwordx4 v[126:129], v67, s[14:15]
	v_lshlrev_b32_e32 v66, 11, v68
	v_and_or_b32 v66, v66, s74, v130
	v_bfe_u32 v67, v68, 16, 16
	v_lshl_or_b32 v67, v67, 11, v130
	global_load_dwordx4 v[98:101], v66, s[14:15]
	global_load_dwordx4 v[102:105], v67, s[14:15]
	v_lshlrev_b32_e32 v66, 11, v69
	v_and_or_b32 v66, v66, s74, v130
	v_bfe_u32 v67, v69, 16, 16
	v_lshl_or_b32 v67, v67, 11, v130
	global_load_dwordx4 v[106:109], v66, s[14:15]
	global_load_dwordx4 v[110:113], v67, s[14:15]
	s_waitcnt vmcnt(22)
	v_perm_b32 v66, v22, v18, s75
	v_perm_b32 v18, v22, v18, s76
	s_waitcnt vmcnt(20)
	v_perm_b32 v22, v30, v26, s75
	v_perm_b32 v26, v30, v26, s76
	v_perm_b32 v30, v22, v66, s77
	v_perm_b32 v22, v22, v66, s78
	v_mov_b32_e32 v69, 0
	s_waitcnt lgkmcnt(0)
	v_dot4c_i32_i8_e32 v69, v22, v70
	v_perm_b32 v22, v26, v18, s77
	v_mov_b32_e32 v73, 0
	v_perm_b32 v18, v26, v18, s78
	v_dot4c_i32_i8_e32 v73, v22, v70
	v_dot4c_i32_i8_e32 v74, v18, v70
	v_perm_b32 v18, v23, v19, s75
	v_perm_b32 v22, v31, v27, s75
	v_perm_b32 v19, v23, v19, s76
	v_perm_b32 v23, v31, v27, s76
	v_perm_b32 v26, v22, v18, s77
	v_perm_b32 v18, v22, v18, s78
	v_dot4c_i32_i8_e32 v76, v18, v70
	v_perm_b32 v18, v23, v19, s77
	v_mov_b32_e32 v77, 0
	v_dot4c_i32_i8_e32 v77, v18, v70
	v_perm_b32 v18, v23, v19, s78
	v_mov_b32_e32 v78, 0
	v_dot4c_i32_i8_e32 v78, v18, v70
	v_perm_b32 v18, v24, v20, s75
	v_perm_b32 v19, v24, v20, s76
	v_perm_b32 v20, v32, v28, s75
	v_perm_b32 v22, v32, v28, s76
	v_perm_b32 v23, v20, v18, s77
	v_perm_b32 v18, v20, v18, s78
	v_mov_b32_e32 v80, 0
	v_dot4c_i32_i8_e32 v80, v18, v70
	v_perm_b32 v18, v22, v19, s77
	v_mov_b32_e32 v81, 0
	v_dot4c_i32_i8_e32 v81, v18, v70
	v_perm_b32 v18, v22, v19, s78
	v_mov_b32_e32 v82, 0
	v_dot4c_i32_i8_e32 v82, v18, v70
	v_perm_b32 v18, v25, v21, s75
	v_perm_b32 v20, v33, v29, s75
	v_perm_b32 v19, v25, v21, s76
	v_perm_b32 v21, v33, v29, s76
	v_perm_b32 v22, v20, v18, s77
	v_perm_b32 v18, v20, v18, s78
	v_mov_b32_e32 v84, 0
	v_dot4c_i32_i8_e32 v84, v18, v70
	v_perm_b32 v18, v21, v19, s77
	v_mov_b32_e32 v85, 0
	v_dot4c_i32_i8_e32 v85, v18, v70
	v_perm_b32 v18, v21, v19, s78
	v_mov_b32_e32 v86, 0
	v_dot4c_i32_i8_e32 v86, v18, v70
	s_waitcnt vmcnt(18)
	v_perm_b32 v18, v6, v2, s75
	v_perm_b32 v2, v6, v2, s76
	s_waitcnt vmcnt(16)
	v_perm_b32 v6, v14, v10, s75
	v_perm_b32 v10, v14, v10, s76
	v_perm_b32 v14, v6, v18, s77
	v_perm_b32 v6, v6, v18, s78
	v_dot4c_i32_i8_e32 v69, v6, v71
	v_perm_b32 v6, v10, v2, s77
	v_perm_b32 v2, v10, v2, s78
	v_dot4c_i32_i8_e32 v73, v6, v71
	v_dot4c_i32_i8_e32 v74, v2, v71
	v_perm_b32 v2, v7, v3, s75
	v_perm_b32 v6, v15, v11, s75
	v_perm_b32 v3, v7, v3, s76
	v_perm_b32 v7, v15, v11, s76
	v_perm_b32 v10, v6, v2, s77
	v_perm_b32 v2, v6, v2, s78
	v_dot4c_i32_i8_e32 v76, v2, v71
	v_perm_b32 v2, v7, v3, s77
	v_dot4c_i32_i8_e32 v77, v2, v71
	v_perm_b32 v2, v7, v3, s78
	v_dot4c_i32_i8_e32 v78, v2, v71
	v_perm_b32 v2, v8, v4, s75
	v_perm_b32 v3, v8, v4, s76
	v_perm_b32 v4, v16, v12, s75
	s_add_i32 s14, s23, 24
	v_perm_b32 v6, v16, v12, s76
	v_perm_b32 v7, v4, v2, s77
	v_perm_b32 v2, v4, v2, s78
	s_and_b32 s14, s14, 0xf80
	v_dot4c_i32_i8_e32 v80, v2, v71
	v_perm_b32 v2, v6, v3, s77
	s_add_u32 s14, s18, s14
	v_dot4c_i32_i8_e32 v81, v2, v71
	v_perm_b32 v2, v6, v3, s78
	s_addc_u32 s15, s19, 0
	s_add_i32 s45, s46, 0xffffff00
	v_mov_b32_e32 v75, 0
	v_dot4c_i32_i8_e32 v82, v2, v71
	v_perm_b32 v2, v9, v5, s75
	v_perm_b32 v4, v17, v13, s75
	s_and_b32 s45, s45, 0x380
	v_dot4c_i32_i8_e32 v75, v26, v70
	v_perm_b32 v6, v4, v2, s77
	v_perm_b32 v2, v4, v2, s78
	v_lshl_add_u32 v4, s45, 1, v181
	v_dot4c_i32_i8_e32 v75, v10, v71
	v_perm_b32 v3, v9, v5, s76
	ds_read_b128 v[8:11], v4 offset:128
	ds_read_b64 v[66:67], v72 offset:64
	v_perm_b32 v5, v17, v13, s76
	v_mov_b32_e32 v68, 0
	v_mov_b32_e32 v79, 0
	v_mov_b32_e32 v83, 0
	v_dot4c_i32_i8_e32 v84, v2, v71
	v_perm_b32 v2, v5, v3, s77
	v_dot4c_i32_i8_e32 v68, v30, v70
	v_dot4c_i32_i8_e32 v79, v23, v70
	v_dot4c_i32_i8_e32 v83, v22, v70
	v_dot4c_i32_i8_e32 v85, v2, v71
	v_perm_b32 v2, v5, v3, s78
	s_waitcnt vmcnt(14)
	v_perm_b32 v70, v54, v50, s75
	s_waitcnt vmcnt(12)
	v_perm_b32 v72, v62, v58, s75
	v_dot4c_i32_i8_e32 v68, v14, v71
	v_dot4c_i32_i8_e32 v79, v7, v71
	v_dot4c_i32_i8_e32 v83, v6, v71
	v_dot4c_i32_i8_e32 v86, v2, v71
	v_perm_b32 v71, v54, v50, s76
	v_perm_b32 v87, v62, v58, s76
	v_perm_b32 v88, v72, v70, s77
	v_perm_b32 v70, v72, v70, s78
	s_waitcnt lgkmcnt(0)
	v_dot4c_i32_i8_e32 v69, v70, v66
	v_perm_b32 v70, v87, v71, s77
	v_dot4c_i32_i8_e32 v73, v70, v66
	v_perm_b32 v70, v87, v71, s78
	v_dot4c_i32_i8_e32 v74, v70, v66
	v_perm_b32 v70, v55, v51, s75
	v_perm_b32 v72, v63, v59, s75
	v_dot4c_i32_i8_e32 v68, v88, v66
	v_perm_b32 v71, v55, v51, s76
	v_perm_b32 v87, v63, v59, s76
	v_perm_b32 v88, v72, v70, s77
	v_perm_b32 v70, v72, v70, s78
	v_dot4c_i32_i8_e32 v76, v70, v66
	v_perm_b32 v70, v87, v71, s77
	v_dot4c_i32_i8_e32 v77, v70, v66
	v_perm_b32 v70, v87, v71, s78
	v_dot4c_i32_i8_e32 v78, v70, v66
	v_perm_b32 v70, v56, v52, s75
	v_perm_b32 v72, v64, v60, s75
	v_dot4c_i32_i8_e32 v75, v88, v66
	v_perm_b32 v71, v56, v52, s76
	v_perm_b32 v87, v64, v60, s76
	v_perm_b32 v88, v72, v70, s77
	v_perm_b32 v70, v72, v70, s78
	v_dot4c_i32_i8_e32 v80, v70, v66
	v_perm_b32 v70, v87, v71, s77
	v_lshlrev_b32_e32 v2, 11, v8
	v_bfe_u32 v3, v8, 16, 16
	v_dot4c_i32_i8_e32 v81, v70, v66
	v_perm_b32 v70, v87, v71, s78
	v_and_or_b32 v2, v2, s74, v130
	v_lshl_or_b32 v3, v3, 11, v130
	v_dot4c_i32_i8_e32 v82, v70, v66
	v_perm_b32 v70, v57, v53, s75
	v_perm_b32 v72, v65, v61, s75
	global_load_dwordx4 v[18:21], v2, s[14:15]
	global_load_dwordx4 v[22:25], v3, s[14:15]
	v_lshlrev_b32_e32 v2, 11, v9
	v_bfe_u32 v3, v9, 16, 16
	v_dot4c_i32_i8_e32 v79, v88, v66
	v_perm_b32 v71, v57, v53, s76
	v_perm_b32 v87, v65, v61, s76
	v_perm_b32 v88, v72, v70, s77
	v_perm_b32 v70, v72, v70, s78
	v_and_or_b32 v2, v2, s74, v130
	v_lshl_or_b32 v3, v3, 11, v130
	v_dot4c_i32_i8_e32 v84, v70, v66
	v_perm_b32 v70, v87, v71, s77
	global_load_dwordx4 v[26:29], v2, s[14:15]
	global_load_dwordx4 v[30:33], v3, s[14:15]
	v_lshlrev_b32_e32 v2, 11, v10
	v_bfe_u32 v3, v10, 16, 16
	v_lshlrev_b32_e32 v10, 11, v11
	v_bfe_u32 v11, v11, 16, 16
	v_dot4c_i32_i8_e32 v85, v70, v66
	v_perm_b32 v70, v87, v71, s78
	v_and_or_b32 v2, v2, s74, v130
	v_lshl_or_b32 v6, v3, 11, v130
	v_and_or_b32 v10, v10, s74, v130
	v_lshl_or_b32 v14, v11, 11, v130
	v_dot4c_i32_i8_e32 v83, v88, v66
	v_dot4c_i32_i8_e32 v86, v70, v66
	s_waitcnt vmcnt(14)
	v_perm_b32 v66, v38, v34, s75
	s_waitcnt vmcnt(12)
	v_perm_b32 v71, v46, v42, s75
	global_load_dwordx4 v[2:5], v2, s[14:15]
	s_nop 0
	global_load_dwordx4 v[6:9], v6, s[14:15]
	s_nop 0
	global_load_dwordx4 v[10:13], v10, s[14:15]
	s_nop 0
	global_load_dwordx4 v[14:17], v14, s[14:15]
	v_perm_b32 v70, v38, v34, s76
	v_perm_b32 v72, v46, v42, s76
	v_perm_b32 v87, v71, v66, s77
	v_perm_b32 v66, v71, v66, s78
	s_or_b32 s15, s44, s29
	v_dot4c_i32_i8_e32 v69, v66, v67
	v_perm_b32 v66, v72, v70, s77
	s_add_i32 s14, s15, s22
	s_lshl_b32 s15, s15, 2
	v_dot4c_i32_i8_e32 v73, v66, v67
	v_perm_b32 v66, v72, v70, s78
	s_add_i32 s15, s15, 0
	v_dot4c_i32_i8_e32 v74, v66, v67
	v_perm_b32 v66, v39, v35, s75
	v_perm_b32 v71, v47, v43, s75
	s_add_i32 s82, s15, 0x14000
	s_ashr_i32 s15, s14, 31
	v_dot4c_i32_i8_e32 v68, v87, v67
	v_perm_b32 v87, v71, v66, s77
	s_and_b32 s44, s23, 0x780
	s_lshl_b64 s[14:15], s[14:15], 12
	v_dot4c_i32_i8_e32 v75, v87, v67
	v_or_b32_e32 v87, s44, v163
	s_add_u32 s44, s60, s14
	s_addc_u32 s45, s61, s15
	v_lshlrev_b32_e32 v88, 1, v87
	v_perm_b32 v70, v39, v35, s76
	v_perm_b32 v72, v47, v43, s76
	v_perm_b32 v66, v71, v66, s78
	v_dot4c_i32_i8_e32 v76, v66, v67
	v_perm_b32 v66, v72, v70, s77
	v_dot4c_i32_i8_e32 v77, v66, v67
	v_perm_b32 v66, v72, v70, s78
	v_dot4c_i32_i8_e32 v78, v66, v67
	v_perm_b32 v66, v40, v36, s75
	v_perm_b32 v71, v48, v44, s75
	v_perm_b32 v70, v40, v36, s76
	v_perm_b32 v72, v48, v44, s76
	v_perm_b32 v90, v71, v66, s77
	v_perm_b32 v66, v71, v66, s78
	v_dot4c_i32_i8_e32 v80, v66, v67
	v_perm_b32 v66, v72, v70, s77
	v_dot4c_i32_i8_e32 v81, v66, v67
	v_perm_b32 v66, v72, v70, s78
	v_dot4c_i32_i8_e32 v82, v66, v67
	v_perm_b32 v66, v41, v37, s75
	v_perm_b32 v71, v49, v45, s75
	v_dot4c_i32_i8_e32 v79, v90, v67
	v_perm_b32 v70, v41, v37, s76
	v_perm_b32 v72, v49, v45, s76
	v_perm_b32 v90, v71, v66, s77
	v_perm_b32 v66, v71, v66, s78
	v_dot4c_i32_i8_e32 v84, v66, v67
	v_perm_b32 v66, v72, v70, s77
	v_dot4c_i32_i8_e32 v85, v66, v67
	v_perm_b32 v66, v72, v70, s78
	v_dot4c_i32_i8_e32 v83, v90, v67
	v_dot4c_i32_i8_e32 v86, v66, v67
	v_permlane32_swap_b32_e32 v68, v79
	v_permlane32_swap_b32_e32 v69, v80
	v_permlane32_swap_b32_e32 v73, v81
	v_permlane32_swap_b32_e32 v74, v82
	v_permlane32_swap_b32_e32 v75, v83
	v_permlane32_swap_b32_e32 v76, v84
	v_permlane32_swap_b32_e32 v77, v85
	v_permlane32_swap_b32_e32 v78, v86
	v_add_u32_e32 v67, v68, v79
	v_add_u32_e32 v68, v69, v80
	v_add_u32_e32 v69, v73, v81
	v_add_u32_e32 v70, v74, v82
	v_add_u32_e32 v71, v75, v83
	v_add_u32_e32 v72, v76, v84
	v_add_u32_e32 v73, v77, v85
	v_add_u32_e32 v74, v78, v86
	v_permlane16_swap_b32_e32 v67, v71
	v_permlane16_swap_b32_e32 v68, v72
	v_permlane16_swap_b32_e32 v69, v73
	v_permlane16_swap_b32_e32 v70, v74
	v_add_u32_e32 v68, v68, v72
	v_add_u32_e32 v67, v67, v71
	v_add_u32_e32 v70, v70, v74
	v_add_u32_e32 v69, v69, v73
	v_mov_b32_e32 v66, s82
	v_cndmask_b32_e64 v71, v67, v69, s[12:13]
	v_cndmask_b32_e64 v72, v70, v68, s[12:13]
	v_cndmask_b32_e64 v67, v69, v67, s[12:13]
	v_cndmask_b32_e64 v68, v68, v70, s[12:13]
	ds_read_b32 v66, v66
	v_lshl_add_u32 v75, v87, 2, 0
	v_add_u32_dpp v67, v71, v67 row_ror:8 row_mask:0xf bank_mask:0xf bound_ctrl:1
	v_add_u32_dpp v70, v68, v72 row_ror:8 row_mask:0xf bank_mask:0xf bound_ctrl:1
	ds_read_b64 v[68:69], v75 offset:32768
	v_cvt_f32_i32_e32 v71, v70
	v_cvt_f32_i32_e32 v70, v67
	s_waitcnt vmcnt(0)
	v_lshlrev_b32_e32 v72, 16, v209
	v_and_b32_e32 v73, 0xffff0000, v209
	s_add_i32 s14, s47, 1
	s_waitcnt lgkmcnt(1)
	v_pk_mul_f32 v[66:67], v[66:67], v[70:71] op_sel_hi:[0,1]
	s_waitcnt lgkmcnt(0)
	v_pk_fma_f32 v[66:67], v[66:67], v[68:69], v[72:73]
	s_and_b32 s82, s14, 7
	v_and_b32_sdwa v69, v66, v199 dst_sel:DWORD dst_unused:UNUSED_PAD src0_sel:WORD_1 src1_sel:DWORD
	v_and_b32_sdwa v68, v67, v199 dst_sel:DWORD dst_unused:UNUSED_PAD src0_sel:WORD_1 src1_sel:DWORD
	v_add3_u32 v66, v66, v69, s80
	v_add3_u32 v67, v67, v68, s80
	v_lshrrev_b32_e32 v66, 16, v66
	v_and_or_b32 v66, v67, s79, v66
	s_cmp_lg_u32 s82, 0
	global_store_dword v88, v66, s[44:45]
	s_cbranch_scc1 .LBB0_1326
	s_lshr_b32 s14, s14, 3
	s_xor_b32 s14, s14, s62
	s_bitcmp0_b32 s14, 0
	s_mov_b64 s[14:15], -1
	s_cbranch_scc1 .LBB0_1324
	s_setprio 1
	s_mov_b64 s[14:15], 0

.LBB0_1326:
	s_or_b32 s84, s82, s29
	s_add_i32 s84, s84, s22
	s_ashr_i32 s85, s84, 31
	s_lshl_b64 s[84:85], s[84:85], 12
	s_add_u32 s84, s60, s84
	s_addc_u32 s85, s61, s85
	s_add_i32 s86, s23, 16
	s_and_b32 s86, s86, 0xf80
	v_or_b32_e32 v210, s86, v163
	v_lshlrev_b32_e32 v210, 1, v210
	global_load_dword v211, v210, s[84:85]
	s_cmpk_lt_u32 s47, 0x7e
	s_cselect_b64 s[44:45], -1, 0
	s_cmpk_gt_u32 s47, 0x7d
	s_cbranch_scc1 .LBB0_1328
	s_add_i32 s14, s23, 32
	s_and_b32 s14, s14, 0xf80
	s_add_u32 s14, s18, s14
	s_addc_u32 s15, s19, 0
	s_add_i32 s83, s46, 0xffffff40
	s_and_b32 s83, s83, 0x380
	v_lshl_add_u32 v34, s83, 1, v181
	ds_read_b128 v[40:43], v34
	s_waitcnt lgkmcnt(0)
	v_lshlrev_b32_e32 v34, 11, v40
	v_bfe_u32 v35, v40, 16, 16
	v_and_or_b32 v34, v34, s74, v130
	v_lshl_or_b32 v35, v35, 11, v130
	global_load_dwordx4 v[50:53], v34, s[14:15]
	global_load_dwordx4 v[54:57], v35, s[14:15]
	v_lshlrev_b32_e32 v34, 11, v41
	v_bfe_u32 v35, v41, 16, 16
	v_and_or_b32 v34, v34, s74, v130
	v_lshl_or_b32 v35, v35, 11, v130
	global_load_dwordx4 v[58:61], v34, s[14:15]
	global_load_dwordx4 v[62:65], v35, s[14:15]
	v_lshlrev_b32_e32 v34, 11, v42
	v_bfe_u32 v35, v42, 16, 16
	v_lshlrev_b32_e32 v42, 11, v43
	v_bfe_u32 v43, v43, 16, 16
	v_and_or_b32 v34, v34, s74, v130
	v_lshl_or_b32 v38, v35, 11, v130
	v_and_or_b32 v42, v42, s74, v130
	v_lshl_or_b32 v46, v43, 11, v130
	global_load_dwordx4 v[34:37], v34, s[14:15]
	s_nop 0
	global_load_dwordx4 v[38:41], v38, s[14:15]
	s_nop 0
	global_load_dwordx4 v[42:45], v42, s[14:15]
	s_nop 0
	global_load_dwordx4 v[46:49], v46, s[14:15]

.LBB0_1330:
	v_perm_b32 v202, v118, v114, s75
	v_perm_b32 v114, v118, v114, s76
	v_perm_b32 v118, v126, v122, s75
	v_perm_b32 v122, v126, v122, s76
	v_perm_b32 v126, v118, v202, s77
	v_mov_b32_e32 v203, 0
	s_waitcnt lgkmcnt(0)
	v_dot4c_i32_i8_e32 v203, v126, v156
	v_perm_b32 v118, v118, v202, s78
	v_mov_b32_e32 v126, 0
	v_dot4c_i32_i8_e32 v126, v118, v156
	v_perm_b32 v118, v122, v114, s77
	v_mov_b32_e32 v202, 0
	v_dot4c_i32_i8_e32 v202, v118, v156
	v_perm_b32 v114, v122, v114, s78
	v_mov_b32_e32 v118, 0
	v_dot4c_i32_i8_e32 v118, v114, v156
	v_perm_b32 v114, v119, v115, s75
	v_perm_b32 v115, v119, v115, s76
	v_perm_b32 v119, v127, v123, s75
	v_perm_b32 v122, v127, v123, s76
	v_perm_b32 v123, v119, v114, s77
	v_mov_b32_e32 v127, 0
	v_perm_b32 v114, v119, v114, s78
	v_mov_b32_e32 v119, 0
	v_dot4c_i32_i8_e32 v127, v123, v156
	v_dot4c_i32_i8_e32 v119, v114, v156
	v_perm_b32 v114, v122, v115, s77
	v_mov_b32_e32 v123, 0
	v_dot4c_i32_i8_e32 v123, v114, v156
	v_perm_b32 v114, v122, v115, s78
	v_mov_b32_e32 v115, 0
	v_dot4c_i32_i8_e32 v115, v114, v156
	v_perm_b32 v114, v120, v116, s75
	v_perm_b32 v116, v120, v116, s76
	v_perm_b32 v120, v128, v124, s75
	v_perm_b32 v122, v128, v124, s76
	v_perm_b32 v124, v120, v114, s77
	v_mov_b32_e32 v128, 0
	v_perm_b32 v114, v120, v114, s78
	v_mov_b32_e32 v120, 0
	v_dot4c_i32_i8_e32 v128, v124, v156
	v_dot4c_i32_i8_e32 v120, v114, v156
	v_perm_b32 v114, v122, v116, s77
	v_mov_b32_e32 v124, 0
	v_dot4c_i32_i8_e32 v124, v114, v156
	v_perm_b32 v114, v122, v116, s78
	v_mov_b32_e32 v116, 0
	v_dot4c_i32_i8_e32 v116, v114, v156
	v_perm_b32 v114, v121, v117, s75
	v_perm_b32 v117, v121, v117, s76
	v_perm_b32 v121, v129, v125, s75
	v_perm_b32 v122, v129, v125, s76
	v_perm_b32 v125, v121, v114, s77
	v_mov_b32_e32 v129, 0
	v_perm_b32 v114, v121, v114, s78
	v_mov_b32_e32 v121, 0
	v_dot4c_i32_i8_e32 v129, v125, v156
	v_dot4c_i32_i8_e32 v121, v114, v156
	v_perm_b32 v114, v122, v117, s77
	v_mov_b32_e32 v125, 0
	v_dot4c_i32_i8_e32 v125, v114, v156
	v_perm_b32 v114, v122, v117, s78
	v_mov_b32_e32 v117, 0
	v_dot4c_i32_i8_e32 v117, v114, v156
	v_perm_b32 v114, v102, v98, s75
	v_perm_b32 v98, v102, v98, s76
	v_perm_b32 v102, v110, v106, s75
	v_perm_b32 v106, v110, v106, s76
	v_perm_b32 v110, v102, v114, s77
	v_perm_b32 v102, v102, v114, s78
	v_dot4c_i32_i8_e32 v126, v102, v157
	v_perm_b32 v102, v106, v98, s77
	v_perm_b32 v98, v106, v98, s78
	v_dot4c_i32_i8_e32 v202, v102, v157
	v_dot4c_i32_i8_e32 v118, v98, v157
	v_perm_b32 v98, v103, v99, s75
	v_perm_b32 v102, v111, v107, s75
	v_perm_b32 v99, v103, v99, s76
	v_perm_b32 v103, v111, v107, s76
	v_perm_b32 v106, v102, v98, s77
	v_perm_b32 v98, v102, v98, s78
	v_dot4c_i32_i8_e32 v119, v98, v157
	v_perm_b32 v98, v103, v99, s77
	v_dot4c_i32_i8_e32 v123, v98, v157
	v_perm_b32 v98, v103, v99, s78
	v_dot4c_i32_i8_e32 v115, v98, v157
	v_perm_b32 v98, v104, v100, s75
	v_perm_b32 v99, v104, v100, s76
	v_perm_b32 v100, v112, v108, s75
	v_perm_b32 v102, v112, v108, s76
	v_perm_b32 v103, v100, v98, s77
	v_perm_b32 v98, v100, v98, s78
	v_dot4c_i32_i8_e32 v120, v98, v157
	v_perm_b32 v98, v102, v99, s77
	v_dot4c_i32_i8_e32 v124, v98, v157
	v_perm_b32 v98, v102, v99, s78
	v_dot4c_i32_i8_e32 v116, v98, v157
	v_perm_b32 v98, v105, v101, s75
	v_perm_b32 v100, v113, v109, s75
	v_perm_b32 v99, v105, v101, s76
	v_perm_b32 v101, v113, v109, s76
	v_perm_b32 v102, v100, v98, s77
	v_perm_b32 v98, v100, v98, s78
	v_dot4c_i32_i8_e32 v121, v98, v157
	v_perm_b32 v98, v101, v99, s77
	v_dot4c_i32_i8_e32 v125, v98, v157
	v_perm_b32 v98, v101, v99, s78
	v_dot4c_i32_i8_e32 v117, v98, v157
	ds_read_b64 v[98:99], v201 offset:64
	v_dot4c_i32_i8_e32 v129, v102, v157
	v_perm_b32 v100, v22, v18, s75
	v_perm_b32 v102, v30, v26, s75
	v_dot4c_i32_i8_e32 v128, v103, v157
	v_perm_b32 v101, v22, v18, s76
	v_perm_b32 v103, v30, v26, s76
	v_perm_b32 v104, v102, v100, s77
	v_perm_b32 v100, v102, v100, s78
	s_waitcnt lgkmcnt(0)
	v_dot4c_i32_i8_e32 v126, v100, v98
	v_perm_b32 v100, v103, v101, s77
	v_dot4c_i32_i8_e32 v202, v100, v98
	v_perm_b32 v100, v103, v101, s78
	v_dot4c_i32_i8_e32 v203, v110, v157
	v_dot4c_i32_i8_e32 v118, v100, v98
	v_perm_b32 v100, v23, v19, s75
	v_perm_b32 v102, v31, v27, s75
	v_dot4c_i32_i8_e32 v203, v104, v98
	v_perm_b32 v101, v23, v19, s76
	v_perm_b32 v103, v31, v27, s76
	v_perm_b32 v104, v102, v100, s77
	v_perm_b32 v100, v102, v100, s78
	v_dot4c_i32_i8_e32 v119, v100, v98
	v_perm_b32 v100, v103, v101, s77
	v_dot4c_i32_i8_e32 v123, v100, v98
	v_perm_b32 v100, v103, v101, s78
	v_dot4c_i32_i8_e32 v127, v106, v157
	v_dot4c_i32_i8_e32 v115, v100, v98
	v_perm_b32 v100, v24, v20, s75
	v_perm_b32 v102, v32, v28, s75
	v_dot4c_i32_i8_e32 v127, v104, v98
	v_perm_b32 v101, v24, v20, s76
	v_perm_b32 v103, v32, v28, s76
	v_perm_b32 v104, v102, v100, s77
	v_perm_b32 v100, v102, v100, s78
	v_dot4c_i32_i8_e32 v120, v100, v98
	v_perm_b32 v100, v103, v101, s77
	v_dot4c_i32_i8_e32 v124, v100, v98
	v_perm_b32 v100, v103, v101, s78
	v_dot4c_i32_i8_e32 v116, v100, v98
	v_perm_b32 v100, v25, v21, s75
	v_perm_b32 v102, v33, v29, s75
	v_dot4c_i32_i8_e32 v128, v104, v98
	v_perm_b32 v101, v25, v21, s76
	v_perm_b32 v103, v33, v29, s76
	v_perm_b32 v104, v102, v100, s77
	v_perm_b32 v100, v102, v100, s78
	v_dot4c_i32_i8_e32 v121, v100, v98
	v_perm_b32 v100, v103, v101, s77
	v_dot4c_i32_i8_e32 v125, v100, v98
	v_perm_b32 v100, v103, v101, s78
	v_dot4c_i32_i8_e32 v129, v104, v98
	v_dot4c_i32_i8_e32 v117, v100, v98
	v_perm_b32 v98, v6, v2, s75
	v_perm_b32 v101, v14, v10, s75
	v_perm_b32 v100, v6, v2, s76
	v_perm_b32 v102, v14, v10, s76
	v_perm_b32 v103, v101, v98, s77
	v_perm_b32 v98, v101, v98, s78
	v_dot4c_i32_i8_e32 v126, v98, v99
	v_perm_b32 v98, v102, v100, s77
	v_dot4c_i32_i8_e32 v202, v98, v99
	v_perm_b32 v98, v102, v100, s78
	s_or_b32 s45, s82, s29
	v_dot4c_i32_i8_e32 v118, v98, v99
	v_perm_b32 v98, v7, v3, s75
	v_perm_b32 v101, v15, v11, s75
	s_add_i32 s44, s45, s22
	s_lshl_b32 s45, s45, 2
	v_dot4c_i32_i8_e32 v203, v103, v99
	v_perm_b32 v103, v101, v98, s77
	s_add_i32 s45, s45, 0
	v_dot4c_i32_i8_e32 v127, v103, v99
	v_or_b32_e32 v103, s81, v163
	s_add_i32 s81, s45, 0x14000
	s_ashr_i32 s45, s44, 31
	s_lshl_b64 s[44:45], s[44:45], 12
	s_add_u32 s44, s60, s44
	s_addc_u32 s45, s61, s45
	v_lshlrev_b32_e32 v106, 1, v103
	v_perm_b32 v100, v7, v3, s76
	v_perm_b32 v102, v15, v11, s76
	v_perm_b32 v98, v101, v98, s78
	v_dot4c_i32_i8_e32 v119, v98, v99
	v_perm_b32 v98, v102, v100, s77
	v_dot4c_i32_i8_e32 v123, v98, v99
	v_perm_b32 v98, v102, v100, s78
	v_dot4c_i32_i8_e32 v115, v98, v99
	v_perm_b32 v98, v8, v4, s75
	v_perm_b32 v101, v16, v12, s75
	v_perm_b32 v100, v8, v4, s76
	v_perm_b32 v102, v16, v12, s76
	v_perm_b32 v104, v101, v98, s77
	v_perm_b32 v98, v101, v98, s78
	v_dot4c_i32_i8_e32 v120, v98, v99
	v_perm_b32 v98, v102, v100, s77
	v_dot4c_i32_i8_e32 v124, v98, v99
	v_perm_b32 v98, v102, v100, s78
	v_dot4c_i32_i8_e32 v116, v98, v99
	v_perm_b32 v98, v9, v5, s75
	v_perm_b32 v101, v17, v13, s75
	v_dot4c_i32_i8_e32 v128, v104, v99
	v_perm_b32 v100, v9, v5, s76
	v_perm_b32 v102, v17, v13, s76
	v_perm_b32 v104, v101, v98, s77
	v_perm_b32 v98, v101, v98, s78
	v_dot4c_i32_i8_e32 v121, v98, v99
	v_perm_b32 v98, v102, v100, s77
	v_dot4c_i32_i8_e32 v125, v98, v99
	v_perm_b32 v98, v102, v100, s78
	v_dot4c_i32_i8_e32 v129, v104, v99
	v_dot4c_i32_i8_e32 v117, v98, v99
	v_permlane32_swap_b32_e32 v203, v128
	v_permlane32_swap_b32_e32 v126, v120
	v_permlane32_swap_b32_e32 v202, v124
	v_permlane32_swap_b32_e32 v118, v116
	v_permlane32_swap_b32_e32 v127, v129
	v_permlane32_swap_b32_e32 v119, v121
	v_permlane32_swap_b32_e32 v123, v125
	v_permlane32_swap_b32_e32 v115, v117
	v_add_u32_e32 v99, v203, v128
	v_add_u32_e32 v100, v126, v120
	v_add_u32_e32 v101, v202, v124
	v_add_u32_e32 v102, v118, v116
	v_add_u32_e32 v104, v127, v129
	v_add_u32_e32 v107, v119, v121
	v_add_u32_e32 v108, v123, v125
	v_add_u32_e32 v109, v115, v117
	v_permlane16_swap_b32_e32 v99, v104
	v_permlane16_swap_b32_e32 v100, v107
	v_permlane16_swap_b32_e32 v101, v108
	v_permlane16_swap_b32_e32 v102, v109
	v_add_u32_e32 v100, v100, v107
	v_add_u32_e32 v99, v99, v104
	v_add_u32_e32 v102, v102, v109
	v_add_u32_e32 v101, v101, v108
	v_mov_b32_e32 v98, s81
	v_cndmask_b32_e64 v104, v99, v101, s[12:13]
	v_cndmask_b32_e64 v107, v102, v100, s[12:13]
	v_cndmask_b32_e64 v99, v101, v99, s[12:13]
	v_cndmask_b32_e64 v100, v100, v102, s[12:13]
	ds_read_b32 v98, v98
	v_lshl_add_u32 v103, v103, 2, 0
	v_add_u32_dpp v99, v104, v99 row_ror:8 row_mask:0xf bank_mask:0xf bound_ctrl:1
	v_add_u32_dpp v102, v100, v107 row_ror:8 row_mask:0xf bank_mask:0xf bound_ctrl:1
	ds_read_b64 v[100:101], v103 offset:32768
	v_cvt_f32_i32_e32 v103, v102
	v_cvt_f32_i32_e32 v102, v99
	s_waitcnt vmcnt(0)
	v_lshlrev_b32_e32 v104, 16, v211
	v_and_b32_e32 v105, 0xffff0000, v211
	s_and_b64 vcc, exec, s[14:15]
	s_waitcnt lgkmcnt(1)
	v_pk_mul_f32 v[98:99], v[98:99], v[102:103] op_sel_hi:[0,1]
	s_waitcnt lgkmcnt(0)
	v_pk_fma_f32 v[98:99], v[98:99], v[100:101], v[104:105]
	s_nop 0
	v_and_b32_sdwa v101, v98, v199 dst_sel:DWORD dst_unused:UNUSED_PAD src0_sel:WORD_1 src1_sel:DWORD
	v_and_b32_sdwa v100, v99, v199 dst_sel:DWORD dst_unused:UNUSED_PAD src0_sel:WORD_1 src1_sel:DWORD
	v_add3_u32 v98, v98, v101, s80
	v_add3_u32 v99, v99, v100, s80
	v_lshrrev_b32_e32 v98, 16, v98
	v_and_or_b32 v98, v99, s79, v98
	global_store_dword v106, v98, s[44:45]
	s_cbranch_vccnz .LBB0_1315
	s_add_i32 s14, s47, 2
	s_and_b32 s44, s14, 7
	s_cmp_lg_u32 s44, 0
	s_cbranch_scc1 .LBB0_1336
	s_lshr_b32 s14, s14, 3
	s_xor_b32 s14, s14, s62
	s_bitcmp0_b32 s14, 0
	s_mov_b64 s[14:15], -1
	s_cbranch_scc1 .LBB0_1334
	s_setprio 1
	s_mov_b64 s[14:15], 0

.LBB0_1336:
	s_or_b32 s84, s44, s29
	s_add_i32 s84, s84, s22
	s_ashr_i32 s85, s84, 31
	s_lshl_b64 s[84:85], s[84:85], 12
	s_add_u32 s84, s60, s84
	s_addc_u32 s85, s61, s85
	s_add_i32 s86, s23, 32
	s_and_b32 s86, s86, 0xf80
	v_or_b32_e32 v212, s86, v163
	v_lshlrev_b32_e32 v212, 1, v212
	global_load_dword v213, v212, s[84:85]
	s_cmpk_lg_i32 s23, 0x7d0
	s_cselect_b64 s[14:15], -1, 0
	s_cmpk_eq_i32 s23, 0x7d0
	s_cbranch_scc1 .LBB0_1338
	s_add_i32 s45, s23, 48
	s_and_b32 s45, s45, 0xf80
	s_add_u32 s82, s18, s45
	s_addc_u32 s83, s19, 0
	s_sub_i32 s45, s46, 64
	s_and_b32 s45, s45, 0x380
	v_lshl_add_u32 v2, s45, 1, v181
	ds_read_b128 v[8:11], v2
	s_waitcnt lgkmcnt(0)
	v_lshlrev_b32_e32 v2, 11, v8
	v_bfe_u32 v3, v8, 16, 16
	v_and_or_b32 v2, v2, s74, v130
	v_lshl_or_b32 v3, v3, 11, v130
	global_load_dwordx4 v[18:21], v2, s[82:83]
	global_load_dwordx4 v[22:25], v3, s[82:83]
	v_lshlrev_b32_e32 v2, 11, v9
	v_bfe_u32 v3, v9, 16, 16
	v_and_or_b32 v2, v2, s74, v130
	v_lshl_or_b32 v3, v3, 11, v130
	global_load_dwordx4 v[26:29], v2, s[82:83]
	global_load_dwordx4 v[30:33], v3, s[82:83]
	v_lshlrev_b32_e32 v2, 11, v10
	v_bfe_u32 v3, v10, 16, 16
	v_lshlrev_b32_e32 v10, 11, v11
	v_bfe_u32 v11, v11, 16, 16
	v_and_or_b32 v2, v2, s74, v130
	v_lshl_or_b32 v6, v3, 11, v130
	v_and_or_b32 v10, v10, s74, v130
	v_lshl_or_b32 v14, v11, 11, v130
	global_load_dwordx4 v[2:5], v2, s[82:83]
	s_nop 0
	global_load_dwordx4 v[6:9], v6, s[82:83]
	s_nop 0
	global_load_dwordx4 v[10:13], v10, s[82:83]
	s_nop 0
	global_load_dwordx4 v[14:17], v14, s[82:83]
